# v9 + first K-loop trip peeled with SrcC=0 on the first MFMA of each accumulator; the 128 v_mov zero-initialisations per unit removed (w1, HGRN, KVQ GEMMs)
# speedup vs baseline: 1.0037x; 1.0037x over previous
.LBB0_170:
	s_ashr_i32 s55, s54, 31
	s_lshl_b64 s[56:57], s[54:55], 20
	s_add_u32 s56, s12, s56
	s_addc_u32 s57, s13, s57
	s_and_b64 s[58:59], s[42:43], exec
	s_cselect_b32 s15, s57, s63
	s_cselect_b32 s29, s56, s62
	s_ashr_i32 s53, s52, 31
	s_lshl_b64 s[58:59], s[52:53], 20
	s_add_u32 s58, s20, s58
	s_addc_u32 s59, s21, s59
	s_and_b64 s[66:67], s[42:43], exec
	s_cselect_b32 s53, s59, s65
	s_cselect_b32 s55, s58, s64
	s_add_u32 s62, s62, 0xc000
	s_addc_u32 s63, s63, 0
	s_add_u32 s61, s64, 0x10000
	s_addc_u32 vcc_lo, s65, 0
	s_mov_b32 vcc_hi, -2
	s_waitcnt lgkmcnt(0)
	s_add_u32 s16, s62, 0x4000
	s_addc_u32 s17, s63, 0
	s_cmp_eq_u32 vcc_hi, 28
	s_cselect_b32 s68, s29, s16
	s_cselect_b32 s69, s15, s17
	s_cselect_b32 s67, s53, vcc_lo
	s_cselect_b32 s66, s55, s61
	s_add_u32 s64, s68, 0x8000
	s_addc_u32 s65, s69, 0
	s_add_i32 s16, 0, 0x10000
	s_add_i32 s17, 0, 0x14000
	v_add_u32_e32 v94, s16, v182
	v_add_u32_e32 v114, s17, v182
	ds_read_b128 v[82:85], v94
	ds_read_b128 v[86:89], v94 offset:1024
	ds_read_b128 v[90:93], v94 offset:2048
	ds_read_b128 v[94:97], v94 offset:3072
	ds_read_b128 v[174:177], v114
	ds_read_b128 v[178:181], v114 offset:1024
	ds_read_b128 v[214:217], v114 offset:2048
	ds_read_b128 v[218:221], v114 offset:3072
	v_lshl_add_u64 v[158:159], s[62:63], 0, v[170:171]
	s_add_i32 m0, s37, 0xc000
	ds_read_b128 v[222:225], v212
	ds_read_b128 v[226:229], v212 offset:1024
	ds_read_b128 v[230:233], v212 offset:2048
	ds_read_b128 v[234:237], v212 offset:3072
	ds_read_b128 v[238:241], v212 offset:4096
	ds_read_b128 v[242:245], v212 offset:5120
	ds_read_b128 v[246:249], v212 offset:6144
	ds_read_b128 v[250:253], v212 offset:7168
	global_load_lds_dwordx4 v[158:159], off
	v_lshl_add_u64 v[158:159], s[62:63], 0, v[172:173]
	s_add_i32 m0, s37, 0xe000
	s_nop 0
	global_load_lds_dwordx4 v[158:159], off
	s_waitcnt vmcnt(8)
	s_waitcnt lgkmcnt(0)
	s_barrier
	s_setprio 1
	s_waitcnt lgkmcnt(0)
	v_mfma_f32_16x16x32_bf16 v[144:147], v[82:85], v[222:225], 0
	v_mfma_f32_16x16x32_bf16 v[140:143], v[90:93], v[222:225], 0
	v_mfma_f32_16x16x32_bf16 v[128:131], v[82:85], v[230:233], 0
	v_mfma_f32_16x16x32_bf16 v[124:127], v[90:93], v[230:233], 0
	v_mfma_f32_16x16x32_bf16 v[110:113], v[82:85], v[238:241], 0
	v_mfma_f32_16x16x32_bf16 v[106:109], v[90:93], v[238:241], 0
	v_mfma_f32_16x16x32_bf16 v[78:81], v[82:85], v[246:249], 0
	v_mfma_f32_16x16x32_bf16 v[74:77], v[90:93], v[246:249], 0
	v_mfma_f32_16x16x32_bf16 v[144:147], v[86:89], v[226:229], v[144:147]
	v_mfma_f32_16x16x32_bf16 v[140:143], v[94:97], v[226:229], v[140:143]
	v_mfma_f32_16x16x32_bf16 v[128:131], v[86:89], v[234:237], v[128:131]
	v_mfma_f32_16x16x32_bf16 v[124:127], v[94:97], v[234:237], v[124:127]
	v_mfma_f32_16x16x32_bf16 v[110:113], v[86:89], v[242:245], v[110:113]
	v_mfma_f32_16x16x32_bf16 v[106:109], v[94:97], v[242:245], v[106:109]
	v_mfma_f32_16x16x32_bf16 v[78:81], v[86:89], v[250:253], v[78:81]
	v_mfma_f32_16x16x32_bf16 v[74:77], v[94:97], v[250:253], v[74:77]
	s_setprio 0
	s_setprio 1
	v_mfma_f32_16x16x32_bf16 v[136:139], v[174:177], v[222:225], 0
	v_mfma_f32_16x16x32_bf16 v[132:135], v[214:217], v[222:225], 0
	v_mfma_f32_16x16x32_bf16 v[120:123], v[174:177], v[230:233], 0
	v_mfma_f32_16x16x32_bf16 v[116:119], v[214:217], v[230:233], 0
	v_mfma_f32_16x16x32_bf16 v[102:105], v[174:177], v[238:241], 0
	v_mfma_f32_16x16x32_bf16 v[98:101], v[214:217], v[238:241], 0
	v_mfma_f32_16x16x32_bf16 v[70:73], v[174:177], v[246:249], 0
	v_mfma_f32_16x16x32_bf16 v[66:69], v[214:217], v[246:249], 0
	v_mfma_f32_16x16x32_bf16 v[136:139], v[178:181], v[226:229], v[136:139]
	v_mfma_f32_16x16x32_bf16 v[132:135], v[218:221], v[226:229], v[132:135]
	v_mfma_f32_16x16x32_bf16 v[120:123], v[178:181], v[234:237], v[120:123]
	v_mfma_f32_16x16x32_bf16 v[116:119], v[218:221], v[234:237], v[116:119]
	v_mfma_f32_16x16x32_bf16 v[102:105], v[178:181], v[242:245], v[102:105]
	v_mfma_f32_16x16x32_bf16 v[98:101], v[218:221], v[242:245], v[98:101]
	v_mfma_f32_16x16x32_bf16 v[70:73], v[178:181], v[250:253], v[70:73]
	v_mfma_f32_16x16x32_bf16 v[66:69], v[218:221], v[250:253], v[66:69]
	s_setprio 0
	s_barrier
	s_add_i32 s16, s16, s9
	v_lshl_add_u64 v[158:159], s[66:67], 0, v[150:151]
	s_mov_b32 m0, s16
	ds_read_b128 v[222:225], v212 offset:16384
	ds_read_b128 v[226:229], v212 offset:17408
	ds_read_b128 v[230:233], v212 offset:18432
	ds_read_b128 v[234:237], v212 offset:19456
	ds_read_b128 v[238:241], v212 offset:20480
	ds_read_b128 v[242:245], v212 offset:21504
	ds_read_b128 v[246:249], v212 offset:22528
	ds_read_b128 v[250:253], v212 offset:23552
	global_load_lds_dwordx4 v[158:159], off
	s_add_i32 m0, s16, 0x2000
	s_add_u32 s26, s66, 0x1000
	v_lshl_add_u64 v[158:159], s[66:67], 0, v[154:155]
	s_addc_u32 s27, s67, 0
	s_add_i32 s16, s17, s9
	global_load_lds_dwordx4 v[158:159], off
	v_lshl_add_u64 v[158:159], s[26:27], 0, v[150:151]
	s_mov_b32 m0, s16
	s_nop 0
	global_load_lds_dwordx4 v[158:159], off
	v_lshl_add_u64 v[158:159], s[26:27], 0, v[154:155]
	s_add_i32 m0, s16, 0x2000
	s_nop 0
	global_load_lds_dwordx4 v[158:159], off
	v_lshl_add_u64 v[158:159], s[68:69], 0, v[148:149]
	s_mov_b32 m0, s37
	s_nop 0
	global_load_lds_dwordx4 v[158:159], off
	v_lshl_add_u64 v[158:159], s[68:69], 0, v[152:153]
	s_mov_b32 m0, s70
	s_nop 0
	global_load_lds_dwordx4 v[158:159], off
	s_waitcnt vmcnt(8)
	s_waitcnt lgkmcnt(0)
	s_barrier
	s_setprio 1
	s_waitcnt lgkmcnt(0)
	v_mfma_f32_16x16x32_bf16 v[62:65], v[82:85], v[222:225], 0
	v_mfma_f32_16x16x32_bf16 v[58:61], v[90:93], v[222:225], 0
	v_mfma_f32_16x16x32_bf16 v[46:49], v[82:85], v[230:233], 0
	v_mfma_f32_16x16x32_bf16 v[42:45], v[90:93], v[230:233], 0
	v_mfma_f32_16x16x32_bf16 v[30:33], v[82:85], v[238:241], 0
	v_mfma_f32_16x16x32_bf16 v[26:29], v[90:93], v[238:241], 0
	v_mfma_f32_16x16x32_bf16 v[14:17], v[82:85], v[246:249], 0
	v_mfma_f32_16x16x32_bf16 v[10:13], v[90:93], v[246:249], 0
	v_mfma_f32_16x16x32_bf16 v[62:65], v[86:89], v[226:229], v[62:65]
	v_mfma_f32_16x16x32_bf16 v[58:61], v[94:97], v[226:229], v[58:61]
	v_mfma_f32_16x16x32_bf16 v[46:49], v[86:89], v[234:237], v[46:49]
	v_mfma_f32_16x16x32_bf16 v[42:45], v[94:97], v[234:237], v[42:45]
	v_mfma_f32_16x16x32_bf16 v[30:33], v[86:89], v[242:245], v[30:33]
	v_mfma_f32_16x16x32_bf16 v[26:29], v[94:97], v[242:245], v[26:29]
	v_mfma_f32_16x16x32_bf16 v[14:17], v[86:89], v[250:253], v[14:17]
	v_mfma_f32_16x16x32_bf16 v[10:13], v[94:97], v[250:253], v[10:13]
	s_setprio 0
	s_setprio 1
	v_mfma_f32_16x16x32_bf16 v[54:57], v[174:177], v[222:225], 0
	v_mfma_f32_16x16x32_bf16 v[50:53], v[214:217], v[222:225], 0
	v_mfma_f32_16x16x32_bf16 v[38:41], v[174:177], v[230:233], 0
	v_mfma_f32_16x16x32_bf16 v[34:37], v[214:217], v[230:233], 0
	v_mfma_f32_16x16x32_bf16 v[22:25], v[174:177], v[238:241], 0
	v_mfma_f32_16x16x32_bf16 v[18:21], v[214:217], v[238:241], 0
	v_mfma_f32_16x16x32_bf16 v[6:9], v[174:177], v[246:249], 0
	v_mfma_f32_16x16x32_bf16 v[2:5], v[214:217], v[246:249], 0
	v_mfma_f32_16x16x32_bf16 v[54:57], v[178:181], v[226:229], v[54:57]
	v_mfma_f32_16x16x32_bf16 v[50:53], v[218:221], v[226:229], v[50:53]
	v_mfma_f32_16x16x32_bf16 v[38:41], v[178:181], v[234:237], v[38:41]
	v_mfma_f32_16x16x32_bf16 v[34:37], v[218:221], v[234:237], v[34:37]
	v_mfma_f32_16x16x32_bf16 v[22:25], v[178:181], v[242:245], v[22:25]
	v_mfma_f32_16x16x32_bf16 v[18:21], v[218:221], v[242:245], v[18:21]
	v_mfma_f32_16x16x32_bf16 v[6:9], v[178:181], v[250:253], v[6:9]
	v_mfma_f32_16x16x32_bf16 v[2:5], v[218:221], v[250:253], v[2:5]
	s_setprio 0
	s_barrier
	s_add_i32 s16, 0, 0x18000
	s_add_i32 s17, 0, 0x1c000
	v_add_u32_e32 v94, s16, v182
	v_add_u32_e32 v114, s17, v182
	ds_read_b128 v[82:85], v94
	ds_read_b128 v[86:89], v94 offset:1024
	ds_read_b128 v[90:93], v94 offset:2048
	ds_read_b128 v[94:97], v94 offset:3072
	ds_read_b128 v[174:177], v114
	ds_read_b128 v[178:181], v114 offset:1024
	ds_read_b128 v[214:217], v114 offset:2048
	ds_read_b128 v[218:221], v114 offset:3072
	s_add_u32 s26, s68, 0x4000
	s_addc_u32 s27, s69, 0
	s_mov_b32 m0, s71
	v_lshl_add_u64 v[158:159], s[26:27], 0, v[148:149]
	ds_read_b128 v[222:225], v212 offset:32768
	ds_read_b128 v[226:229], v212 offset:33792
	ds_read_b128 v[230:233], v212 offset:34816
	ds_read_b128 v[234:237], v212 offset:35840
	ds_read_b128 v[238:241], v212 offset:36864
	ds_read_b128 v[242:245], v212 offset:37888
	ds_read_b128 v[246:249], v212 offset:38912
	ds_read_b128 v[250:253], v212 offset:39936
	global_load_lds_dwordx4 v[158:159], off
	v_lshl_add_u64 v[158:159], s[26:27], 0, v[152:153]
	s_mov_b32 m0, s74
	s_nop 0
	global_load_lds_dwordx4 v[158:159], off
	s_waitcnt vmcnt(8)
	s_waitcnt lgkmcnt(0)
	s_barrier
	s_setprio 1
	s_waitcnt lgkmcnt(0)
	v_mfma_f32_16x16x32_bf16 v[144:147], v[82:85], v[222:225], v[144:147]
	v_mfma_f32_16x16x32_bf16 v[140:143], v[90:93], v[222:225], v[140:143]
	v_mfma_f32_16x16x32_bf16 v[128:131], v[82:85], v[230:233], v[128:131]
	v_mfma_f32_16x16x32_bf16 v[124:127], v[90:93], v[230:233], v[124:127]
	v_mfma_f32_16x16x32_bf16 v[110:113], v[82:85], v[238:241], v[110:113]
	v_mfma_f32_16x16x32_bf16 v[106:109], v[90:93], v[238:241], v[106:109]
	v_mfma_f32_16x16x32_bf16 v[78:81], v[82:85], v[246:249], v[78:81]
	v_mfma_f32_16x16x32_bf16 v[74:77], v[90:93], v[246:249], v[74:77]
	v_mfma_f32_16x16x32_bf16 v[144:147], v[86:89], v[226:229], v[144:147]
	v_mfma_f32_16x16x32_bf16 v[140:143], v[94:97], v[226:229], v[140:143]
	v_mfma_f32_16x16x32_bf16 v[128:131], v[86:89], v[234:237], v[128:131]
	v_mfma_f32_16x16x32_bf16 v[124:127], v[94:97], v[234:237], v[124:127]
	v_mfma_f32_16x16x32_bf16 v[110:113], v[86:89], v[242:245], v[110:113]
	v_mfma_f32_16x16x32_bf16 v[106:109], v[94:97], v[242:245], v[106:109]
	v_mfma_f32_16x16x32_bf16 v[78:81], v[86:89], v[250:253], v[78:81]
	v_mfma_f32_16x16x32_bf16 v[74:77], v[94:97], v[250:253], v[74:77]
	s_setprio 0
	s_setprio 1
	v_mfma_f32_16x16x32_bf16 v[136:139], v[174:177], v[222:225], v[136:139]
	v_mfma_f32_16x16x32_bf16 v[132:135], v[214:217], v[222:225], v[132:135]
	v_mfma_f32_16x16x32_bf16 v[120:123], v[174:177], v[230:233], v[120:123]
	v_mfma_f32_16x16x32_bf16 v[116:119], v[214:217], v[230:233], v[116:119]
	v_mfma_f32_16x16x32_bf16 v[102:105], v[174:177], v[238:241], v[102:105]
	v_mfma_f32_16x16x32_bf16 v[98:101], v[214:217], v[238:241], v[98:101]
	v_mfma_f32_16x16x32_bf16 v[70:73], v[174:177], v[246:249], v[70:73]
	v_mfma_f32_16x16x32_bf16 v[66:69], v[214:217], v[246:249], v[66:69]
	v_mfma_f32_16x16x32_bf16 v[136:139], v[178:181], v[226:229], v[136:139]
	v_mfma_f32_16x16x32_bf16 v[132:135], v[218:221], v[226:229], v[132:135]
	v_mfma_f32_16x16x32_bf16 v[120:123], v[178:181], v[234:237], v[120:123]
	v_mfma_f32_16x16x32_bf16 v[116:119], v[218:221], v[234:237], v[116:119]
	v_mfma_f32_16x16x32_bf16 v[102:105], v[178:181], v[242:245], v[102:105]
	v_mfma_f32_16x16x32_bf16 v[98:101], v[218:221], v[242:245], v[98:101]
	v_mfma_f32_16x16x32_bf16 v[70:73], v[178:181], v[250:253], v[70:73]
	v_mfma_f32_16x16x32_bf16 v[66:69], v[218:221], v[250:253], v[66:69]
	s_setprio 0
	s_barrier
	s_add_u32 s26, s66, 0x8000
	s_addc_u32 s27, s67, 0
	s_add_i32 s16, s16, s9
	v_lshl_add_u64 v[158:159], s[26:27], 0, v[150:151]
	s_mov_b32 m0, s16
	ds_read_b128 v[222:225], v212 offset:49152
	ds_read_b128 v[226:229], v212 offset:50176
	ds_read_b128 v[230:233], v212 offset:51200
	ds_read_b128 v[234:237], v212 offset:52224
	ds_read_b128 v[238:241], v212 offset:53248
	ds_read_b128 v[242:245], v212 offset:54272
	ds_read_b128 v[246:249], v212 offset:55296
	ds_read_b128 v[250:253], v212 offset:56320
	global_load_lds_dwordx4 v[158:159], off
	s_add_i32 m0, s16, 0x2000
	v_lshl_add_u64 v[158:159], s[26:27], 0, v[154:155]
	s_add_u32 s26, s66, 0x9000
	s_addc_u32 s27, s67, 0
	s_add_i32 s16, s17, s9
	global_load_lds_dwordx4 v[158:159], off
	v_lshl_add_u64 v[158:159], s[26:27], 0, v[150:151]
	s_mov_b32 m0, s16
	s_nop 0
	global_load_lds_dwordx4 v[158:159], off
	v_lshl_add_u64 v[158:159], s[26:27], 0, v[154:155]
	s_add_i32 m0, s16, 0x2000
	s_nop 0
	global_load_lds_dwordx4 v[158:159], off
	v_lshl_add_u64 v[158:159], s[64:65], 0, v[148:149]
	s_mov_b32 m0, s86
	s_nop 0
	global_load_lds_dwordx4 v[158:159], off
	v_lshl_add_u64 v[158:159], s[64:65], 0, v[152:153]
	s_mov_b32 m0, s87
	s_nop 0
	global_load_lds_dwordx4 v[158:159], off
	s_waitcnt vmcnt(8)
	s_waitcnt lgkmcnt(0)
	s_barrier
	s_setprio 1
	s_waitcnt lgkmcnt(0)
	v_mfma_f32_16x16x32_bf16 v[62:65], v[82:85], v[222:225], v[62:65]
	v_mfma_f32_16x16x32_bf16 v[58:61], v[90:93], v[222:225], v[58:61]
	v_mfma_f32_16x16x32_bf16 v[46:49], v[82:85], v[230:233], v[46:49]
	v_mfma_f32_16x16x32_bf16 v[42:45], v[90:93], v[230:233], v[42:45]
	v_mfma_f32_16x16x32_bf16 v[30:33], v[82:85], v[238:241], v[30:33]
	v_mfma_f32_16x16x32_bf16 v[26:29], v[90:93], v[238:241], v[26:29]
	v_mfma_f32_16x16x32_bf16 v[14:17], v[82:85], v[246:249], v[14:17]
	v_mfma_f32_16x16x32_bf16 v[10:13], v[90:93], v[246:249], v[10:13]
	v_mfma_f32_16x16x32_bf16 v[62:65], v[86:89], v[226:229], v[62:65]
	v_mfma_f32_16x16x32_bf16 v[58:61], v[94:97], v[226:229], v[58:61]
	v_mfma_f32_16x16x32_bf16 v[46:49], v[86:89], v[234:237], v[46:49]
	v_mfma_f32_16x16x32_bf16 v[42:45], v[94:97], v[234:237], v[42:45]
	v_mfma_f32_16x16x32_bf16 v[30:33], v[86:89], v[242:245], v[30:33]
	v_mfma_f32_16x16x32_bf16 v[26:29], v[94:97], v[242:245], v[26:29]
	v_mfma_f32_16x16x32_bf16 v[14:17], v[86:89], v[250:253], v[14:17]
	v_mfma_f32_16x16x32_bf16 v[10:13], v[94:97], v[250:253], v[10:13]
	s_setprio 0
	s_setprio 1
	v_mfma_f32_16x16x32_bf16 v[54:57], v[174:177], v[222:225], v[54:57]
	v_mfma_f32_16x16x32_bf16 v[50:53], v[214:217], v[222:225], v[50:53]
	v_mfma_f32_16x16x32_bf16 v[38:41], v[174:177], v[230:233], v[38:41]
	v_mfma_f32_16x16x32_bf16 v[34:37], v[214:217], v[230:233], v[34:37]
	v_mfma_f32_16x16x32_bf16 v[22:25], v[174:177], v[238:241], v[22:25]
	v_mfma_f32_16x16x32_bf16 v[18:21], v[214:217], v[238:241], v[18:21]
	v_mfma_f32_16x16x32_bf16 v[6:9], v[174:177], v[246:249], v[6:9]
	v_mfma_f32_16x16x32_bf16 v[2:5], v[214:217], v[246:249], v[2:5]
	v_mfma_f32_16x16x32_bf16 v[54:57], v[178:181], v[226:229], v[54:57]
	v_mfma_f32_16x16x32_bf16 v[50:53], v[218:221], v[226:229], v[50:53]
	v_mfma_f32_16x16x32_bf16 v[38:41], v[178:181], v[234:237], v[38:41]
	v_mfma_f32_16x16x32_bf16 v[34:37], v[218:221], v[234:237], v[34:37]
	v_mfma_f32_16x16x32_bf16 v[22:25], v[178:181], v[242:245], v[22:25]
	v_mfma_f32_16x16x32_bf16 v[18:21], v[218:221], v[242:245], v[18:21]
	v_mfma_f32_16x16x32_bf16 v[6:9], v[178:181], v[250:253], v[6:9]
	v_mfma_f32_16x16x32_bf16 v[2:5], v[218:221], v[250:253], v[2:5]
	s_setprio 0
	s_barrier
	s_add_i32 vcc_hi, vcc_hi, 2
	s_add_u32 s62, s62, 0x10000
	s_addc_u32 s63, s63, 0
	s_add_u32 s61, s61, 0x10000
	s_addc_u32 vcc_lo, vcc_lo, 0
	s_cmp_gt_u32 vcc_hi, 29
	s_cbranch_scc0 .LBB0_171
	s_branch .Lpeel_exit_split

.Lpeel_exit_split:
	s_and_b64 vcc, exec, s[48:49]
	s_cbranch_vccz .LBB0_174
	s_barrier

.LBB0_345:
	s_ashr_i32 s51, s50, 31
	s_lshl_b64 s[52:53], s[50:51], 20
	s_add_u32 s52, s5, s52
	s_addc_u32 s53, s8, s53
	s_and_b64 s[54:55], s[38:39], exec
	s_cselect_b32 s15, s53, s57
	s_cselect_b32 s29, s52, s56
	s_ashr_i32 s49, s48, 31
	s_lshl_b64 s[54:55], s[48:49], 20
	s_add_u32 s54, s9, s54
	s_addc_u32 s55, s12, s55
	s_and_b64 s[60:61], s[38:39], exec
	s_cselect_b32 s41, s55, s59
	s_cselect_b32 s49, s54, s58
	s_add_u32 s56, s56, 0xc000
	s_addc_u32 s57, s57, 0
	s_add_u32 s51, s58, 0x10000
	s_addc_u32 s69, s59, 0
	s_mov_b32 s70, -2
	s_add_u32 s16, s56, 0x4000
	s_addc_u32 s17, s57, 0
	s_cmp_eq_u32 s70, 28
	s_cselect_b32 s62, s29, s16
	s_cselect_b32 s63, s15, s17
	s_cselect_b32 s61, s41, s69
	s_cselect_b32 s60, s49, s51
	s_add_u32 s58, s62, 0x8000
	s_addc_u32 s59, s63, 0
	s_add_i32 s16, 0, 0x10000
	v_add_u32_e32 v114, s16, v172
	s_add_i32 s17, 0, 0x14000
	ds_read_b128 v[132:135], v114
	ds_read_b128 v[136:139], v114 offset:1024
	s_waitcnt lgkmcnt(0)
	ds_read_b128 v[152:155], v114 offset:2048
	ds_read_b128 v[166:169], v114 offset:3072
	v_add_u32_e32 v114, s17, v172
	ds_read_b128 v[176:179], v114
	ds_read_b128 v[180:183], v114 offset:1024
	ds_read_b128 v[194:197], v114 offset:2048
	ds_read_b128 v[198:201], v114 offset:3072
	v_lshl_add_u64 v[158:159], s[56:57], 0, v[148:149]
	s_add_i32 m0, s13, 0xc000
	ds_read_b128 v[202:205], v175
	ds_read_b128 v[206:209], v175 offset:1024
	ds_read_b128 v[210:213], v175 offset:2048
	ds_read_b128 v[214:217], v175 offset:3072
	ds_read_b128 v[218:221], v175 offset:4096
	ds_read_b128 v[222:225], v175 offset:5120
	ds_read_b128 v[226:229], v175 offset:6144
	ds_read_b128 v[230:233], v175 offset:7168
	s_cmp_lg_u32 s32, 0
	s_cbranch_scc1 .Lrxp_hgrn1_skip
	global_load_lds_dwordx4 v[158:159], off
	v_lshl_add_u64 v[158:159], s[56:57], 0, v[150:151]
	s_add_i32 m0, s13, 0xe000
	s_nop 0
	global_load_lds_dwordx4 v[158:159], off

.Lrxp_hgrn1_w0:
	s_waitcnt vmcnt(24)
	s_waitcnt lgkmcnt(0)
	s_barrier
	s_setprio 1
	s_waitcnt lgkmcnt(0)
	v_mfma_f32_16x16x32_bf16 v[128:131], v[132:135], v[202:205], 0
	v_mfma_f32_16x16x32_bf16 v[124:127], v[152:155], v[202:205], 0
	v_mfma_f32_16x16x32_bf16 v[110:113], v[132:135], v[210:213], 0
	v_mfma_f32_16x16x32_bf16 v[106:109], v[152:155], v[210:213], 0
	v_mfma_f32_16x16x32_bf16 v[94:97], v[132:135], v[218:221], 0
	v_mfma_f32_16x16x32_bf16 v[90:93], v[152:155], v[218:221], 0
	v_mfma_f32_16x16x32_bf16 v[78:81], v[132:135], v[226:229], 0
	v_mfma_f32_16x16x32_bf16 v[74:77], v[152:155], v[226:229], 0
	v_mfma_f32_16x16x32_bf16 v[128:131], v[136:139], v[206:209], v[128:131]
	v_mfma_f32_16x16x32_bf16 v[124:127], v[166:169], v[206:209], v[124:127]
	v_mfma_f32_16x16x32_bf16 v[110:113], v[136:139], v[214:217], v[110:113]
	v_mfma_f32_16x16x32_bf16 v[106:109], v[166:169], v[214:217], v[106:109]
	v_mfma_f32_16x16x32_bf16 v[94:97], v[136:139], v[222:225], v[94:97]
	v_mfma_f32_16x16x32_bf16 v[90:93], v[166:169], v[222:225], v[90:93]
	v_mfma_f32_16x16x32_bf16 v[78:81], v[136:139], v[230:233], v[78:81]
	v_mfma_f32_16x16x32_bf16 v[74:77], v[166:169], v[230:233], v[74:77]
	s_setprio 0
	s_setprio 1
	v_mfma_f32_16x16x32_bf16 v[120:123], v[176:179], v[202:205], 0
	v_mfma_f32_16x16x32_bf16 v[116:119], v[194:197], v[202:205], 0
	v_mfma_f32_16x16x32_bf16 v[102:105], v[176:179], v[210:213], 0
	v_mfma_f32_16x16x32_bf16 v[98:101], v[194:197], v[210:213], 0
	v_mfma_f32_16x16x32_bf16 v[86:89], v[176:179], v[218:221], 0
	v_mfma_f32_16x16x32_bf16 v[82:85], v[194:197], v[218:221], 0
	v_mfma_f32_16x16x32_bf16 v[70:73], v[176:179], v[226:229], 0
	v_mfma_f32_16x16x32_bf16 v[66:69], v[194:197], v[226:229], 0
	v_mfma_f32_16x16x32_bf16 v[120:123], v[180:183], v[206:209], v[120:123]
	v_mfma_f32_16x16x32_bf16 v[116:119], v[198:201], v[206:209], v[116:119]
	v_mfma_f32_16x16x32_bf16 v[102:105], v[180:183], v[214:217], v[102:105]
	v_mfma_f32_16x16x32_bf16 v[98:101], v[198:201], v[214:217], v[98:101]
	v_mfma_f32_16x16x32_bf16 v[86:89], v[180:183], v[222:225], v[86:89]
	v_mfma_f32_16x16x32_bf16 v[82:85], v[198:201], v[222:225], v[82:85]
	v_mfma_f32_16x16x32_bf16 v[70:73], v[180:183], v[230:233], v[70:73]
	v_mfma_f32_16x16x32_bf16 v[66:69], v[198:201], v[230:233], v[66:69]
	s_setprio 0
	s_barrier
	s_add_i32 s16, s16, s4
	v_lshl_add_u64 v[158:159], s[60:61], 0, v[142:143]
	s_mov_b32 m0, s16
	ds_read_b128 v[202:205], v175 offset:16384
	ds_read_b128 v[206:209], v175 offset:17408
	ds_read_b128 v[210:213], v175 offset:18432
	ds_read_b128 v[214:217], v175 offset:19456
	ds_read_b128 v[218:221], v175 offset:20480
	ds_read_b128 v[222:225], v175 offset:21504
	ds_read_b128 v[226:229], v175 offset:22528
	ds_read_b128 v[230:233], v175 offset:23552
	global_load_lds_dwordx4 v[158:159], off
	s_add_i32 m0, s16, 0x2000
	s_add_u32 s74, s60, 0x1000
	v_lshl_add_u64 v[158:159], s[60:61], 0, v[146:147]
	s_addc_u32 s75, s61, 0
	s_add_i32 s16, s17, s4
	global_load_lds_dwordx4 v[158:159], off
	v_lshl_add_u64 v[158:159], s[74:75], 0, v[142:143]
	s_mov_b32 m0, s16
	s_nop 0
	global_load_lds_dwordx4 v[158:159], off
	v_lshl_add_u64 v[158:159], s[74:75], 0, v[146:147]
	s_add_i32 m0, s16, 0x2000
	s_nop 0
	global_load_lds_dwordx4 v[158:159], off
	v_lshl_add_u64 v[158:159], s[62:63], 0, v[140:141]
	s_mov_b32 m0, s13
	s_nop 0
	global_load_lds_dwordx4 v[158:159], off
	v_lshl_add_u64 v[158:159], s[62:63], 0, v[144:145]
	s_mov_b32 m0, s20
	s_nop 0
	global_load_lds_dwordx4 v[158:159], off
	s_cmp_lg_u32 s32, 0
	s_cbranch_scc1 .Lrxp_hgrn1_w1
	s_waitcnt vmcnt(8)
.Lrxp_hgrn1_w1:
	s_waitcnt vmcnt(24)
	s_waitcnt lgkmcnt(0)
	s_barrier
	s_setprio 1
	s_waitcnt lgkmcnt(0)
	v_mfma_f32_16x16x32_bf16 v[62:65], v[132:135], v[202:205], 0
	v_mfma_f32_16x16x32_bf16 v[58:61], v[152:155], v[202:205], 0
	v_mfma_f32_16x16x32_bf16 v[46:49], v[132:135], v[210:213], 0
	v_mfma_f32_16x16x32_bf16 v[42:45], v[152:155], v[210:213], 0
	v_mfma_f32_16x16x32_bf16 v[30:33], v[132:135], v[218:221], 0
	v_mfma_f32_16x16x32_bf16 v[26:29], v[152:155], v[218:221], 0
	v_mfma_f32_16x16x32_bf16 v[14:17], v[132:135], v[226:229], 0
	v_mfma_f32_16x16x32_bf16 v[10:13], v[152:155], v[226:229], 0
	v_mfma_f32_16x16x32_bf16 v[62:65], v[136:139], v[206:209], v[62:65]
	v_mfma_f32_16x16x32_bf16 v[58:61], v[166:169], v[206:209], v[58:61]
	v_mfma_f32_16x16x32_bf16 v[46:49], v[136:139], v[214:217], v[46:49]
	v_mfma_f32_16x16x32_bf16 v[42:45], v[166:169], v[214:217], v[42:45]
	v_mfma_f32_16x16x32_bf16 v[30:33], v[136:139], v[222:225], v[30:33]
	v_mfma_f32_16x16x32_bf16 v[26:29], v[166:169], v[222:225], v[26:29]
	v_mfma_f32_16x16x32_bf16 v[14:17], v[136:139], v[230:233], v[14:17]
	v_mfma_f32_16x16x32_bf16 v[10:13], v[166:169], v[230:233], v[10:13]
	s_setprio 0
	s_setprio 1
	v_mfma_f32_16x16x32_bf16 v[54:57], v[176:179], v[202:205], 0
	v_mfma_f32_16x16x32_bf16 v[50:53], v[194:197], v[202:205], 0
	v_mfma_f32_16x16x32_bf16 v[38:41], v[176:179], v[210:213], 0
	v_mfma_f32_16x16x32_bf16 v[34:37], v[194:197], v[210:213], 0
	v_mfma_f32_16x16x32_bf16 v[22:25], v[176:179], v[218:221], 0
	v_mfma_f32_16x16x32_bf16 v[18:21], v[194:197], v[218:221], 0
	v_mfma_f32_16x16x32_bf16 v[6:9], v[176:179], v[226:229], 0
	v_mfma_f32_16x16x32_bf16 v[2:5], v[194:197], v[226:229], 0
	v_mfma_f32_16x16x32_bf16 v[54:57], v[180:183], v[206:209], v[54:57]
	v_mfma_f32_16x16x32_bf16 v[50:53], v[198:201], v[206:209], v[50:53]
	v_mfma_f32_16x16x32_bf16 v[38:41], v[180:183], v[214:217], v[38:41]
	v_mfma_f32_16x16x32_bf16 v[34:37], v[198:201], v[214:217], v[34:37]
	v_mfma_f32_16x16x32_bf16 v[22:25], v[180:183], v[222:225], v[22:25]
	v_mfma_f32_16x16x32_bf16 v[18:21], v[198:201], v[222:225], v[18:21]
	v_mfma_f32_16x16x32_bf16 v[6:9], v[180:183], v[230:233], v[6:9]
	v_mfma_f32_16x16x32_bf16 v[2:5], v[198:201], v[230:233], v[2:5]
	s_setprio 0
	s_barrier
	s_add_i32 s16, 0, 0x18000
	v_add_u32_e32 v114, s16, v172
	s_add_i32 s17, 0, 0x1c000
	ds_read_b128 v[132:135], v114
	ds_read_b128 v[136:139], v114 offset:1024
	ds_read_b128 v[152:155], v114 offset:2048
	ds_read_b128 v[166:169], v114 offset:3072
	v_add_u32_e32 v114, s17, v172
	ds_read_b128 v[176:179], v114
	ds_read_b128 v[180:183], v114 offset:1024
	ds_read_b128 v[194:197], v114 offset:2048
	ds_read_b128 v[198:201], v114 offset:3072
	s_add_u32 s62, s62, 0x4000
	s_addc_u32 s63, s63, 0
	s_mov_b32 m0, s21
	v_lshl_add_u64 v[158:159], s[62:63], 0, v[140:141]
	ds_read_b128 v[202:205], v175 offset:32768
	ds_read_b128 v[206:209], v175 offset:33792
	ds_read_b128 v[210:213], v175 offset:34816
	ds_read_b128 v[214:217], v175 offset:35840
	ds_read_b128 v[218:221], v175 offset:36864
	ds_read_b128 v[222:225], v175 offset:37888
	ds_read_b128 v[226:229], v175 offset:38912
	ds_read_b128 v[230:233], v175 offset:39936
	global_load_lds_dwordx4 v[158:159], off
	v_lshl_add_u64 v[158:159], s[62:63], 0, v[144:145]
	s_mov_b32 m0, s24
	s_nop 0
	global_load_lds_dwordx4 v[158:159], off
	s_cmp_lg_u32 s32, 0
	s_cbranch_scc1 .Lrxp_hgrn1_w2
	s_waitcnt vmcnt(8)
.Lrxp_hgrn1_w2:
	s_waitcnt vmcnt(24)
	s_mov_b32 s32, 0
	s_waitcnt lgkmcnt(0)
	s_barrier
	s_setprio 1
	s_waitcnt lgkmcnt(0)
	v_mfma_f32_16x16x32_bf16 v[128:131], v[132:135], v[202:205], v[128:131]
	v_mfma_f32_16x16x32_bf16 v[124:127], v[152:155], v[202:205], v[124:127]
	v_mfma_f32_16x16x32_bf16 v[110:113], v[132:135], v[210:213], v[110:113]
	v_mfma_f32_16x16x32_bf16 v[106:109], v[152:155], v[210:213], v[106:109]
	v_mfma_f32_16x16x32_bf16 v[94:97], v[132:135], v[218:221], v[94:97]
	v_mfma_f32_16x16x32_bf16 v[90:93], v[152:155], v[218:221], v[90:93]
	v_mfma_f32_16x16x32_bf16 v[78:81], v[132:135], v[226:229], v[78:81]
	v_mfma_f32_16x16x32_bf16 v[74:77], v[152:155], v[226:229], v[74:77]
	v_mfma_f32_16x16x32_bf16 v[128:131], v[136:139], v[206:209], v[128:131]
	v_mfma_f32_16x16x32_bf16 v[124:127], v[166:169], v[206:209], v[124:127]
	v_mfma_f32_16x16x32_bf16 v[110:113], v[136:139], v[214:217], v[110:113]
	v_mfma_f32_16x16x32_bf16 v[106:109], v[166:169], v[214:217], v[106:109]
	v_mfma_f32_16x16x32_bf16 v[94:97], v[136:139], v[222:225], v[94:97]
	v_mfma_f32_16x16x32_bf16 v[90:93], v[166:169], v[222:225], v[90:93]
	v_mfma_f32_16x16x32_bf16 v[78:81], v[136:139], v[230:233], v[78:81]
	v_mfma_f32_16x16x32_bf16 v[74:77], v[166:169], v[230:233], v[74:77]
	s_setprio 0
	s_setprio 1
	v_mfma_f32_16x16x32_bf16 v[120:123], v[176:179], v[202:205], v[120:123]
	v_mfma_f32_16x16x32_bf16 v[116:119], v[194:197], v[202:205], v[116:119]
	v_mfma_f32_16x16x32_bf16 v[102:105], v[176:179], v[210:213], v[102:105]
	v_mfma_f32_16x16x32_bf16 v[98:101], v[194:197], v[210:213], v[98:101]
	v_mfma_f32_16x16x32_bf16 v[86:89], v[176:179], v[218:221], v[86:89]
	v_mfma_f32_16x16x32_bf16 v[82:85], v[194:197], v[218:221], v[82:85]
	v_mfma_f32_16x16x32_bf16 v[70:73], v[176:179], v[226:229], v[70:73]
	v_mfma_f32_16x16x32_bf16 v[66:69], v[194:197], v[226:229], v[66:69]
	v_mfma_f32_16x16x32_bf16 v[120:123], v[180:183], v[206:209], v[120:123]
	v_mfma_f32_16x16x32_bf16 v[116:119], v[198:201], v[206:209], v[116:119]
	v_mfma_f32_16x16x32_bf16 v[102:105], v[180:183], v[214:217], v[102:105]
	v_mfma_f32_16x16x32_bf16 v[98:101], v[198:201], v[214:217], v[98:101]
	v_mfma_f32_16x16x32_bf16 v[86:89], v[180:183], v[222:225], v[86:89]
	v_mfma_f32_16x16x32_bf16 v[82:85], v[198:201], v[222:225], v[82:85]
	v_mfma_f32_16x16x32_bf16 v[70:73], v[180:183], v[230:233], v[70:73]
	v_mfma_f32_16x16x32_bf16 v[66:69], v[198:201], v[230:233], v[66:69]
	s_setprio 0
	s_barrier
	s_add_u32 s62, s60, 0x8000
	s_addc_u32 s63, s61, 0
	s_add_i32 s16, s16, s4
	v_lshl_add_u64 v[158:159], s[62:63], 0, v[142:143]
	s_mov_b32 m0, s16
	ds_read_b128 v[202:205], v175 offset:49152
	ds_read_b128 v[206:209], v175 offset:50176
	ds_read_b128 v[210:213], v175 offset:51200
	ds_read_b128 v[214:217], v175 offset:52224
	ds_read_b128 v[218:221], v175 offset:53248
	ds_read_b128 v[222:225], v175 offset:54272
	ds_read_b128 v[226:229], v175 offset:55296
	ds_read_b128 v[230:233], v175 offset:56320
	global_load_lds_dwordx4 v[158:159], off
	s_add_i32 m0, s16, 0x2000
	s_add_u32 s60, s60, 0x9000
	v_lshl_add_u64 v[158:159], s[62:63], 0, v[146:147]
	s_addc_u32 s61, s61, 0
	s_add_i32 s16, s17, s4
	global_load_lds_dwordx4 v[158:159], off
	v_lshl_add_u64 v[158:159], s[60:61], 0, v[142:143]
	s_mov_b32 m0, s16
	s_nop 0
	global_load_lds_dwordx4 v[158:159], off
	v_lshl_add_u64 v[158:159], s[60:61], 0, v[146:147]
	s_add_i32 m0, s16, 0x2000
	s_nop 0
	global_load_lds_dwordx4 v[158:159], off
	v_lshl_add_u64 v[158:159], s[58:59], 0, v[140:141]
	s_mov_b32 m0, s65
	s_nop 0
	global_load_lds_dwordx4 v[158:159], off
	v_lshl_add_u64 v[158:159], s[58:59], 0, v[144:145]
	s_mov_b32 m0, s66
	s_nop 0
	global_load_lds_dwordx4 v[158:159], off
	s_waitcnt vmcnt(8)
	s_waitcnt lgkmcnt(0)
	s_barrier
	s_setprio 1
	s_waitcnt lgkmcnt(0)
	v_mfma_f32_16x16x32_bf16 v[62:65], v[132:135], v[202:205], v[62:65]
	v_mfma_f32_16x16x32_bf16 v[58:61], v[152:155], v[202:205], v[58:61]
	v_mfma_f32_16x16x32_bf16 v[46:49], v[132:135], v[210:213], v[46:49]
	v_mfma_f32_16x16x32_bf16 v[42:45], v[152:155], v[210:213], v[42:45]
	v_mfma_f32_16x16x32_bf16 v[30:33], v[132:135], v[218:221], v[30:33]
	v_mfma_f32_16x16x32_bf16 v[26:29], v[152:155], v[218:221], v[26:29]
	v_mfma_f32_16x16x32_bf16 v[14:17], v[132:135], v[226:229], v[14:17]
	v_mfma_f32_16x16x32_bf16 v[10:13], v[152:155], v[226:229], v[10:13]
	v_mfma_f32_16x16x32_bf16 v[62:65], v[136:139], v[206:209], v[62:65]
	v_mfma_f32_16x16x32_bf16 v[58:61], v[166:169], v[206:209], v[58:61]
	v_mfma_f32_16x16x32_bf16 v[46:49], v[136:139], v[214:217], v[46:49]
	v_mfma_f32_16x16x32_bf16 v[42:45], v[166:169], v[214:217], v[42:45]
	v_mfma_f32_16x16x32_bf16 v[30:33], v[136:139], v[222:225], v[30:33]
	v_mfma_f32_16x16x32_bf16 v[26:29], v[166:169], v[222:225], v[26:29]
	v_mfma_f32_16x16x32_bf16 v[14:17], v[136:139], v[230:233], v[14:17]
	v_mfma_f32_16x16x32_bf16 v[10:13], v[166:169], v[230:233], v[10:13]
	s_setprio 0
	s_setprio 1
	v_mfma_f32_16x16x32_bf16 v[54:57], v[176:179], v[202:205], v[54:57]
	v_mfma_f32_16x16x32_bf16 v[50:53], v[194:197], v[202:205], v[50:53]
	v_mfma_f32_16x16x32_bf16 v[38:41], v[176:179], v[210:213], v[38:41]
	v_mfma_f32_16x16x32_bf16 v[34:37], v[194:197], v[210:213], v[34:37]
	v_mfma_f32_16x16x32_bf16 v[22:25], v[176:179], v[218:221], v[22:25]
	v_mfma_f32_16x16x32_bf16 v[18:21], v[194:197], v[218:221], v[18:21]
	v_mfma_f32_16x16x32_bf16 v[6:9], v[176:179], v[226:229], v[6:9]
	v_mfma_f32_16x16x32_bf16 v[2:5], v[194:197], v[226:229], v[2:5]
	v_mfma_f32_16x16x32_bf16 v[54:57], v[180:183], v[206:209], v[54:57]
	v_mfma_f32_16x16x32_bf16 v[50:53], v[198:201], v[206:209], v[50:53]
	v_mfma_f32_16x16x32_bf16 v[38:41], v[180:183], v[214:217], v[38:41]
	v_mfma_f32_16x16x32_bf16 v[34:37], v[198:201], v[214:217], v[34:37]
	v_mfma_f32_16x16x32_bf16 v[22:25], v[180:183], v[222:225], v[22:25]
	v_mfma_f32_16x16x32_bf16 v[18:21], v[198:201], v[222:225], v[18:21]
	v_mfma_f32_16x16x32_bf16 v[6:9], v[180:183], v[230:233], v[6:9]
	v_mfma_f32_16x16x32_bf16 v[2:5], v[198:201], v[230:233], v[2:5]
	s_setprio 0
	s_barrier
	s_add_i32 s70, s70, 2
	s_add_u32 s56, s56, 0x10000
	s_addc_u32 s57, s57, 0
	s_add_u32 s51, s51, 0x10000
	s_addc_u32 s69, s69, 0
	s_cmp_gt_u32 s70, 29
	s_cbranch_scc0 .LBB0_346
	s_branch .Lpeel_exit_hgrn1

.Lpeel_exit_hgrn1:
	s_add_u32 s100, s29, 0xc000
	s_addc_u32 s101, s15, 0
	v_lshl_add_u64 v[158:159], s[100:101], 0, v[148:149]
	s_add_i32 m0, s13, 0xc000
	s_nop 0
	global_load_lds_dwordx4 v[158:159], off
	v_lshl_add_u64 v[158:159], s[100:101], 0, v[150:151]
	s_add_i32 m0, s13, 0xe000
	s_nop 0
	global_load_lds_dwordx4 v[158:159], off
	s_and_b64 vcc, exec, s[46:47]
	s_cbranch_vccz .LBB0_349
	s_barrier

.LBB0_502:
	s_ashr_i32 s49, s48, 31
	s_lshl_b64 s[50:51], s[48:49], 20
	s_add_u32 s50, s5, s50
	s_addc_u32 s51, s7, s51
	s_and_b64 s[52:53], s[38:39], exec
	s_cselect_b32 s15, s51, s55
	s_cselect_b32 s29, s50, s54
	s_ashr_i32 s47, s46, 31
	s_lshl_b64 s[52:53], s[46:47], 20
	s_add_u32 s52, s8, s52
	s_addc_u32 s53, s9, s53
	s_and_b64 s[58:59], s[38:39], exec
	s_cselect_b32 s41, s53, s57
	s_cselect_b32 s47, s52, s56
	s_add_u32 s54, s54, 0xc000
	s_addc_u32 s55, s55, 0
	s_add_u32 s49, s56, 0x10000
	s_addc_u32 s66, s57, 0
	s_mov_b32 s67, -2
	s_add_u32 s16, s54, 0x4000
	s_addc_u32 s17, s55, 0
	s_cmp_eq_u32 s67, 28
	s_cselect_b32 s60, s29, s16
	s_cselect_b32 s61, s15, s17
	s_cselect_b32 s59, s41, s66
	s_cselect_b32 s58, s47, s49
	s_add_u32 s56, s60, 0x8000
	s_addc_u32 s57, s61, 0
	s_add_i32 s16, 0, 0x10000
	v_add_u32_e32 v114, s16, v172
	s_add_i32 s17, 0, 0x14000
	ds_read_b128 v[132:135], v114
	ds_read_b128 v[136:139], v114 offset:1024
	s_waitcnt lgkmcnt(0)
	ds_read_b128 v[152:155], v114 offset:2048
	ds_read_b128 v[166:169], v114 offset:3072
	v_add_u32_e32 v114, s17, v172
	ds_read_b128 v[176:179], v114
	ds_read_b128 v[180:183], v114 offset:1024
	ds_read_b128 v[194:197], v114 offset:2048
	ds_read_b128 v[198:201], v114 offset:3072
	v_lshl_add_u64 v[158:159], s[54:55], 0, v[148:149]
	s_add_i32 m0, s12, 0xc000
	ds_read_b128 v[202:205], v175
	ds_read_b128 v[206:209], v175 offset:1024
	ds_read_b128 v[210:213], v175 offset:2048
	ds_read_b128 v[214:217], v175 offset:3072
	ds_read_b128 v[218:221], v175 offset:4096
	ds_read_b128 v[222:225], v175 offset:5120
	ds_read_b128 v[226:229], v175 offset:6144
	ds_read_b128 v[230:233], v175 offset:7168
	s_cmp_lg_u32 s32, 0
	s_cbranch_scc1 .Lrxp_hgrn2_skip
	global_load_lds_dwordx4 v[158:159], off
	v_lshl_add_u64 v[158:159], s[54:55], 0, v[150:151]
	s_add_i32 m0, s12, 0xe000
	s_nop 0
	global_load_lds_dwordx4 v[158:159], off

.Lrxp_hgrn2_w0:
	s_waitcnt vmcnt(24)
	s_waitcnt lgkmcnt(0)
	s_barrier
	s_setprio 1
	s_waitcnt lgkmcnt(0)
	v_mfma_f32_16x16x32_bf16 v[128:131], v[132:135], v[202:205], 0
	v_mfma_f32_16x16x32_bf16 v[124:127], v[152:155], v[202:205], 0
	v_mfma_f32_16x16x32_bf16 v[110:113], v[132:135], v[210:213], 0
	v_mfma_f32_16x16x32_bf16 v[106:109], v[152:155], v[210:213], 0
	v_mfma_f32_16x16x32_bf16 v[94:97], v[132:135], v[218:221], 0
	v_mfma_f32_16x16x32_bf16 v[90:93], v[152:155], v[218:221], 0
	v_mfma_f32_16x16x32_bf16 v[78:81], v[132:135], v[226:229], 0
	v_mfma_f32_16x16x32_bf16 v[74:77], v[152:155], v[226:229], 0
	v_mfma_f32_16x16x32_bf16 v[128:131], v[136:139], v[206:209], v[128:131]
	v_mfma_f32_16x16x32_bf16 v[124:127], v[166:169], v[206:209], v[124:127]
	v_mfma_f32_16x16x32_bf16 v[110:113], v[136:139], v[214:217], v[110:113]
	v_mfma_f32_16x16x32_bf16 v[106:109], v[166:169], v[214:217], v[106:109]
	v_mfma_f32_16x16x32_bf16 v[94:97], v[136:139], v[222:225], v[94:97]
	v_mfma_f32_16x16x32_bf16 v[90:93], v[166:169], v[222:225], v[90:93]
	v_mfma_f32_16x16x32_bf16 v[78:81], v[136:139], v[230:233], v[78:81]
	v_mfma_f32_16x16x32_bf16 v[74:77], v[166:169], v[230:233], v[74:77]
	s_setprio 0
	s_setprio 1
	v_mfma_f32_16x16x32_bf16 v[120:123], v[176:179], v[202:205], 0
	v_mfma_f32_16x16x32_bf16 v[116:119], v[194:197], v[202:205], 0
	v_mfma_f32_16x16x32_bf16 v[102:105], v[176:179], v[210:213], 0
	v_mfma_f32_16x16x32_bf16 v[98:101], v[194:197], v[210:213], 0
	v_mfma_f32_16x16x32_bf16 v[86:89], v[176:179], v[218:221], 0
	v_mfma_f32_16x16x32_bf16 v[82:85], v[194:197], v[218:221], 0
	v_mfma_f32_16x16x32_bf16 v[70:73], v[176:179], v[226:229], 0
	v_mfma_f32_16x16x32_bf16 v[66:69], v[194:197], v[226:229], 0
	v_mfma_f32_16x16x32_bf16 v[120:123], v[180:183], v[206:209], v[120:123]
	v_mfma_f32_16x16x32_bf16 v[116:119], v[198:201], v[206:209], v[116:119]
	v_mfma_f32_16x16x32_bf16 v[102:105], v[180:183], v[214:217], v[102:105]
	v_mfma_f32_16x16x32_bf16 v[98:101], v[198:201], v[214:217], v[98:101]
	v_mfma_f32_16x16x32_bf16 v[86:89], v[180:183], v[222:225], v[86:89]
	v_mfma_f32_16x16x32_bf16 v[82:85], v[198:201], v[222:225], v[82:85]
	v_mfma_f32_16x16x32_bf16 v[70:73], v[180:183], v[230:233], v[70:73]
	v_mfma_f32_16x16x32_bf16 v[66:69], v[198:201], v[230:233], v[66:69]
	s_setprio 0
	s_barrier
	s_add_i32 s16, s16, s4
	v_lshl_add_u64 v[158:159], s[58:59], 0, v[142:143]
	s_mov_b32 m0, s16
	ds_read_b128 v[202:205], v175 offset:16384
	ds_read_b128 v[206:209], v175 offset:17408
	ds_read_b128 v[210:213], v175 offset:18432
	ds_read_b128 v[214:217], v175 offset:19456
	ds_read_b128 v[218:221], v175 offset:20480
	ds_read_b128 v[222:225], v175 offset:21504
	ds_read_b128 v[226:229], v175 offset:22528
	ds_read_b128 v[230:233], v175 offset:23552
	global_load_lds_dwordx4 v[158:159], off
	s_add_i32 m0, s16, 0x2000
	s_add_u32 s68, s58, 0x1000
	v_lshl_add_u64 v[158:159], s[58:59], 0, v[146:147]
	s_addc_u32 s69, s59, 0
	s_add_i32 s16, s17, s4
	global_load_lds_dwordx4 v[158:159], off
	v_lshl_add_u64 v[158:159], s[68:69], 0, v[142:143]
	s_mov_b32 m0, s16
	s_nop 0
	global_load_lds_dwordx4 v[158:159], off
	v_lshl_add_u64 v[158:159], s[68:69], 0, v[146:147]
	s_add_i32 m0, s16, 0x2000
	s_nop 0
	global_load_lds_dwordx4 v[158:159], off
	v_lshl_add_u64 v[158:159], s[60:61], 0, v[140:141]
	s_mov_b32 m0, s12
	s_nop 0
	global_load_lds_dwordx4 v[158:159], off
	v_lshl_add_u64 v[158:159], s[60:61], 0, v[144:145]
	s_mov_b32 m0, s13
	s_nop 0
	global_load_lds_dwordx4 v[158:159], off
	s_cmp_lg_u32 s32, 0
	s_cbranch_scc1 .Lrxp_hgrn2_w1
	s_waitcnt vmcnt(8)
.Lrxp_hgrn2_w1:
	s_waitcnt vmcnt(24)
	s_waitcnt lgkmcnt(0)
	s_barrier
	s_setprio 1
	s_waitcnt lgkmcnt(0)
	v_mfma_f32_16x16x32_bf16 v[62:65], v[132:135], v[202:205], 0
	v_mfma_f32_16x16x32_bf16 v[58:61], v[152:155], v[202:205], 0
	v_mfma_f32_16x16x32_bf16 v[46:49], v[132:135], v[210:213], 0
	v_mfma_f32_16x16x32_bf16 v[42:45], v[152:155], v[210:213], 0
	v_mfma_f32_16x16x32_bf16 v[30:33], v[132:135], v[218:221], 0
	v_mfma_f32_16x16x32_bf16 v[26:29], v[152:155], v[218:221], 0
	v_mfma_f32_16x16x32_bf16 v[14:17], v[132:135], v[226:229], 0
	v_mfma_f32_16x16x32_bf16 v[10:13], v[152:155], v[226:229], 0
	v_mfma_f32_16x16x32_bf16 v[62:65], v[136:139], v[206:209], v[62:65]
	v_mfma_f32_16x16x32_bf16 v[58:61], v[166:169], v[206:209], v[58:61]
	v_mfma_f32_16x16x32_bf16 v[46:49], v[136:139], v[214:217], v[46:49]
	v_mfma_f32_16x16x32_bf16 v[42:45], v[166:169], v[214:217], v[42:45]
	v_mfma_f32_16x16x32_bf16 v[30:33], v[136:139], v[222:225], v[30:33]
	v_mfma_f32_16x16x32_bf16 v[26:29], v[166:169], v[222:225], v[26:29]
	v_mfma_f32_16x16x32_bf16 v[14:17], v[136:139], v[230:233], v[14:17]
	v_mfma_f32_16x16x32_bf16 v[10:13], v[166:169], v[230:233], v[10:13]
	s_setprio 0
	s_setprio 1
	v_mfma_f32_16x16x32_bf16 v[54:57], v[176:179], v[202:205], 0
	v_mfma_f32_16x16x32_bf16 v[50:53], v[194:197], v[202:205], 0
	v_mfma_f32_16x16x32_bf16 v[38:41], v[176:179], v[210:213], 0
	v_mfma_f32_16x16x32_bf16 v[34:37], v[194:197], v[210:213], 0
	v_mfma_f32_16x16x32_bf16 v[22:25], v[176:179], v[218:221], 0
	v_mfma_f32_16x16x32_bf16 v[18:21], v[194:197], v[218:221], 0
	v_mfma_f32_16x16x32_bf16 v[6:9], v[176:179], v[226:229], 0
	v_mfma_f32_16x16x32_bf16 v[2:5], v[194:197], v[226:229], 0
	v_mfma_f32_16x16x32_bf16 v[54:57], v[180:183], v[206:209], v[54:57]
	v_mfma_f32_16x16x32_bf16 v[50:53], v[198:201], v[206:209], v[50:53]
	v_mfma_f32_16x16x32_bf16 v[38:41], v[180:183], v[214:217], v[38:41]
	v_mfma_f32_16x16x32_bf16 v[34:37], v[198:201], v[214:217], v[34:37]
	v_mfma_f32_16x16x32_bf16 v[22:25], v[180:183], v[222:225], v[22:25]
	v_mfma_f32_16x16x32_bf16 v[18:21], v[198:201], v[222:225], v[18:21]
	v_mfma_f32_16x16x32_bf16 v[6:9], v[180:183], v[230:233], v[6:9]
	v_mfma_f32_16x16x32_bf16 v[2:5], v[198:201], v[230:233], v[2:5]
	s_setprio 0
	s_barrier
	s_add_i32 s16, 0, 0x18000
	v_add_u32_e32 v114, s16, v172
	s_add_i32 s17, 0, 0x1c000
	ds_read_b128 v[132:135], v114
	ds_read_b128 v[136:139], v114 offset:1024
	ds_read_b128 v[152:155], v114 offset:2048
	ds_read_b128 v[166:169], v114 offset:3072
	v_add_u32_e32 v114, s17, v172
	ds_read_b128 v[176:179], v114
	ds_read_b128 v[180:183], v114 offset:1024
	ds_read_b128 v[194:197], v114 offset:2048
	ds_read_b128 v[198:201], v114 offset:3072
	s_add_u32 s60, s60, 0x4000
	s_addc_u32 s61, s61, 0
	s_mov_b32 m0, s20
	v_lshl_add_u64 v[158:159], s[60:61], 0, v[140:141]
	ds_read_b128 v[202:205], v175 offset:32768
	ds_read_b128 v[206:209], v175 offset:33792
	ds_read_b128 v[210:213], v175 offset:34816
	ds_read_b128 v[214:217], v175 offset:35840
	ds_read_b128 v[218:221], v175 offset:36864
	ds_read_b128 v[222:225], v175 offset:37888
	ds_read_b128 v[226:229], v175 offset:38912
	ds_read_b128 v[230:233], v175 offset:39936
	global_load_lds_dwordx4 v[158:159], off
	v_lshl_add_u64 v[158:159], s[60:61], 0, v[144:145]
	s_mov_b32 m0, s21
	s_nop 0
	global_load_lds_dwordx4 v[158:159], off
	s_cmp_lg_u32 s32, 0
	s_cbranch_scc1 .Lrxp_hgrn2_w2
	s_waitcnt vmcnt(8)
.Lrxp_hgrn2_w2:
	s_waitcnt vmcnt(24)
	s_mov_b32 s32, 0
	s_waitcnt lgkmcnt(0)
	s_barrier
	s_setprio 1
	s_waitcnt lgkmcnt(0)
	v_mfma_f32_16x16x32_bf16 v[128:131], v[132:135], v[202:205], v[128:131]
	v_mfma_f32_16x16x32_bf16 v[124:127], v[152:155], v[202:205], v[124:127]
	v_mfma_f32_16x16x32_bf16 v[110:113], v[132:135], v[210:213], v[110:113]
	v_mfma_f32_16x16x32_bf16 v[106:109], v[152:155], v[210:213], v[106:109]
	v_mfma_f32_16x16x32_bf16 v[94:97], v[132:135], v[218:221], v[94:97]
	v_mfma_f32_16x16x32_bf16 v[90:93], v[152:155], v[218:221], v[90:93]
	v_mfma_f32_16x16x32_bf16 v[78:81], v[132:135], v[226:229], v[78:81]
	v_mfma_f32_16x16x32_bf16 v[74:77], v[152:155], v[226:229], v[74:77]
	v_mfma_f32_16x16x32_bf16 v[128:131], v[136:139], v[206:209], v[128:131]
	v_mfma_f32_16x16x32_bf16 v[124:127], v[166:169], v[206:209], v[124:127]
	v_mfma_f32_16x16x32_bf16 v[110:113], v[136:139], v[214:217], v[110:113]
	v_mfma_f32_16x16x32_bf16 v[106:109], v[166:169], v[214:217], v[106:109]
	v_mfma_f32_16x16x32_bf16 v[94:97], v[136:139], v[222:225], v[94:97]
	v_mfma_f32_16x16x32_bf16 v[90:93], v[166:169], v[222:225], v[90:93]
	v_mfma_f32_16x16x32_bf16 v[78:81], v[136:139], v[230:233], v[78:81]
	v_mfma_f32_16x16x32_bf16 v[74:77], v[166:169], v[230:233], v[74:77]
	s_setprio 0
	s_setprio 1
	v_mfma_f32_16x16x32_bf16 v[120:123], v[176:179], v[202:205], v[120:123]
	v_mfma_f32_16x16x32_bf16 v[116:119], v[194:197], v[202:205], v[116:119]
	v_mfma_f32_16x16x32_bf16 v[102:105], v[176:179], v[210:213], v[102:105]
	v_mfma_f32_16x16x32_bf16 v[98:101], v[194:197], v[210:213], v[98:101]
	v_mfma_f32_16x16x32_bf16 v[86:89], v[176:179], v[218:221], v[86:89]
	v_mfma_f32_16x16x32_bf16 v[82:85], v[194:197], v[218:221], v[82:85]
	v_mfma_f32_16x16x32_bf16 v[70:73], v[176:179], v[226:229], v[70:73]
	v_mfma_f32_16x16x32_bf16 v[66:69], v[194:197], v[226:229], v[66:69]
	v_mfma_f32_16x16x32_bf16 v[120:123], v[180:183], v[206:209], v[120:123]
	v_mfma_f32_16x16x32_bf16 v[116:119], v[198:201], v[206:209], v[116:119]
	v_mfma_f32_16x16x32_bf16 v[102:105], v[180:183], v[214:217], v[102:105]
	v_mfma_f32_16x16x32_bf16 v[98:101], v[198:201], v[214:217], v[98:101]
	v_mfma_f32_16x16x32_bf16 v[86:89], v[180:183], v[222:225], v[86:89]
	v_mfma_f32_16x16x32_bf16 v[82:85], v[198:201], v[222:225], v[82:85]
	v_mfma_f32_16x16x32_bf16 v[70:73], v[180:183], v[230:233], v[70:73]
	v_mfma_f32_16x16x32_bf16 v[66:69], v[198:201], v[230:233], v[66:69]
	s_setprio 0
	s_barrier
	s_add_u32 s60, s58, 0x8000
	s_addc_u32 s61, s59, 0
	s_add_i32 s16, s16, s4
	v_lshl_add_u64 v[158:159], s[60:61], 0, v[142:143]
	s_mov_b32 m0, s16
	ds_read_b128 v[202:205], v175 offset:49152
	ds_read_b128 v[206:209], v175 offset:50176
	ds_read_b128 v[210:213], v175 offset:51200
	ds_read_b128 v[214:217], v175 offset:52224
	ds_read_b128 v[218:221], v175 offset:53248
	ds_read_b128 v[222:225], v175 offset:54272
	ds_read_b128 v[226:229], v175 offset:55296
	ds_read_b128 v[230:233], v175 offset:56320
	global_load_lds_dwordx4 v[158:159], off
	s_add_i32 m0, s16, 0x2000
	s_add_u32 s58, s58, 0x9000
	v_lshl_add_u64 v[158:159], s[60:61], 0, v[146:147]
	s_addc_u32 s59, s59, 0
	s_add_i32 s16, s17, s4
	global_load_lds_dwordx4 v[158:159], off
	v_lshl_add_u64 v[158:159], s[58:59], 0, v[142:143]
	s_mov_b32 m0, s16
	s_nop 0
	global_load_lds_dwordx4 v[158:159], off
	v_lshl_add_u64 v[158:159], s[58:59], 0, v[146:147]
	s_add_i32 m0, s16, 0x2000
	s_nop 0
	global_load_lds_dwordx4 v[158:159], off
	v_lshl_add_u64 v[158:159], s[56:57], 0, v[140:141]
	s_mov_b32 m0, s62
	s_nop 0
	global_load_lds_dwordx4 v[158:159], off
	v_lshl_add_u64 v[158:159], s[56:57], 0, v[144:145]
	s_mov_b32 m0, s63
	s_nop 0
	global_load_lds_dwordx4 v[158:159], off
	s_waitcnt vmcnt(8)
	s_waitcnt lgkmcnt(0)
	s_barrier
	s_setprio 1
	s_waitcnt lgkmcnt(0)
	v_mfma_f32_16x16x32_bf16 v[62:65], v[132:135], v[202:205], v[62:65]
	v_mfma_f32_16x16x32_bf16 v[58:61], v[152:155], v[202:205], v[58:61]
	v_mfma_f32_16x16x32_bf16 v[46:49], v[132:135], v[210:213], v[46:49]
	v_mfma_f32_16x16x32_bf16 v[42:45], v[152:155], v[210:213], v[42:45]
	v_mfma_f32_16x16x32_bf16 v[30:33], v[132:135], v[218:221], v[30:33]
	v_mfma_f32_16x16x32_bf16 v[26:29], v[152:155], v[218:221], v[26:29]
	v_mfma_f32_16x16x32_bf16 v[14:17], v[132:135], v[226:229], v[14:17]
	v_mfma_f32_16x16x32_bf16 v[10:13], v[152:155], v[226:229], v[10:13]
	v_mfma_f32_16x16x32_bf16 v[62:65], v[136:139], v[206:209], v[62:65]
	v_mfma_f32_16x16x32_bf16 v[58:61], v[166:169], v[206:209], v[58:61]
	v_mfma_f32_16x16x32_bf16 v[46:49], v[136:139], v[214:217], v[46:49]
	v_mfma_f32_16x16x32_bf16 v[42:45], v[166:169], v[214:217], v[42:45]
	v_mfma_f32_16x16x32_bf16 v[30:33], v[136:139], v[222:225], v[30:33]
	v_mfma_f32_16x16x32_bf16 v[26:29], v[166:169], v[222:225], v[26:29]
	v_mfma_f32_16x16x32_bf16 v[14:17], v[136:139], v[230:233], v[14:17]
	v_mfma_f32_16x16x32_bf16 v[10:13], v[166:169], v[230:233], v[10:13]
	s_setprio 0
	s_setprio 1
	v_mfma_f32_16x16x32_bf16 v[54:57], v[176:179], v[202:205], v[54:57]
	v_mfma_f32_16x16x32_bf16 v[50:53], v[194:197], v[202:205], v[50:53]
	v_mfma_f32_16x16x32_bf16 v[38:41], v[176:179], v[210:213], v[38:41]
	v_mfma_f32_16x16x32_bf16 v[34:37], v[194:197], v[210:213], v[34:37]
	v_mfma_f32_16x16x32_bf16 v[22:25], v[176:179], v[218:221], v[22:25]
	v_mfma_f32_16x16x32_bf16 v[18:21], v[194:197], v[218:221], v[18:21]
	v_mfma_f32_16x16x32_bf16 v[6:9], v[176:179], v[226:229], v[6:9]
	v_mfma_f32_16x16x32_bf16 v[2:5], v[194:197], v[226:229], v[2:5]
	v_mfma_f32_16x16x32_bf16 v[54:57], v[180:183], v[206:209], v[54:57]
	v_mfma_f32_16x16x32_bf16 v[50:53], v[198:201], v[206:209], v[50:53]
	v_mfma_f32_16x16x32_bf16 v[38:41], v[180:183], v[214:217], v[38:41]
	v_mfma_f32_16x16x32_bf16 v[34:37], v[198:201], v[214:217], v[34:37]
	v_mfma_f32_16x16x32_bf16 v[22:25], v[180:183], v[222:225], v[22:25]
	v_mfma_f32_16x16x32_bf16 v[18:21], v[198:201], v[222:225], v[18:21]
	v_mfma_f32_16x16x32_bf16 v[6:9], v[180:183], v[230:233], v[6:9]
	v_mfma_f32_16x16x32_bf16 v[2:5], v[198:201], v[230:233], v[2:5]
	s_setprio 0
	s_barrier
	s_add_i32 s67, s67, 2
	s_add_u32 s54, s54, 0x10000
	s_addc_u32 s55, s55, 0
	s_add_u32 s49, s49, 0x10000
	s_addc_u32 s66, s66, 0
	s_cmp_gt_u32 s67, 29
	s_cbranch_scc0 .LBB0_503
	s_branch .Lpeel_exit_hgrn2

.Lpeel_exit_hgrn2:
	s_add_u32 s100, s29, 0xc000
	s_addc_u32 s101, s15, 0
	v_lshl_add_u64 v[158:159], s[100:101], 0, v[148:149]
	s_add_i32 m0, s12, 0xc000
	s_nop 0
	global_load_lds_dwordx4 v[158:159], off
	v_lshl_add_u64 v[158:159], s[100:101], 0, v[150:151]
	s_add_i32 m0, s12, 0xe000
	s_nop 0
	global_load_lds_dwordx4 v[158:159], off
	s_and_b64 vcc, exec, s[44:45]
	s_cbranch_vccz .LBB0_506
	s_barrier

.LBB0_1229:
	s_ashr_i32 s29, s28, 31
	s_lshl_b64 s[16:17], s[28:29], 20
	s_add_u32 s40, s12, s16
	s_addc_u32 s41, s13, s17
	s_and_b64 s[16:17], s[38:39], exec
	s_cselect_b32 s29, s41, s47
	s_cselect_b32 s60, s40, s46
	s_ashr_i32 s27, s26, 31
	s_lshl_b64 s[16:17], s[26:27], 20
	s_add_u32 s42, s14, s16
	s_addc_u32 s43, s15, s17
	s_and_b64 s[16:17], s[38:39], exec
	s_cselect_b32 s27, s43, s49
	s_cselect_b32 s61, s42, s48
	s_add_u32 s46, s46, 0xc000
	s_addc_u32 s47, s47, 0
	s_add_u32 s62, s48, 0x10000
	s_addc_u32 s63, s49, 0
	s_mov_b32 s64, -2
	s_add_u32 s16, s46, 0x4000
	s_addc_u32 s17, s47, 0
	s_cmp_eq_u32 s64, 28
	s_cselect_b32 s52, s60, s16
	s_cselect_b32 s53, s29, s17
	s_cselect_b32 s51, s27, s63
	s_cselect_b32 s50, s61, s62
	s_add_u32 s48, s52, 0x8000
	s_addc_u32 s49, s53, 0
	s_add_i32 s16, 0, 0x10000
	v_add_u32_e32 v144, s16, v1
	s_add_i32 s65, 0, 0x14000
	ds_read_b128 v[148:151], v144
	ds_read_b128 v[152:155], v144 offset:1024
	ds_read_b128 v[158:161], v144 offset:2048
	ds_read_b128 v[166:169], v144 offset:3072
	v_add_u32_e32 v144, s65, v1
	ds_read_b128 v[170:173], v144
	ds_read_b128 v[174:177], v144 offset:1024
	ds_read_b128 v[178:181], v144 offset:2048
	ds_read_b128 v[194:197], v144 offset:3072
	v_lshl_add_u64 v[144:145], s[46:47], 0, v[140:141]
	s_add_i32 m0, s20, 0xc000
	ds_read_b128 v[198:201], v147
	ds_read_b128 v[202:205], v147 offset:1024
	ds_read_b128 v[206:209], v147 offset:2048
	ds_read_b128 v[210:213], v147 offset:3072
	ds_read_b128 v[214:217], v147 offset:4096
	ds_read_b128 v[218:221], v147 offset:5120
	ds_read_b128 v[222:225], v147 offset:6144
	ds_read_b128 v[226:229], v147 offset:7168
	s_cmp_lg_u32 s32, 0
	s_cbranch_scc1 .Lrxp_relu2_skip
	global_load_lds_dwordx4 v[144:145], off
	v_lshl_add_u64 v[144:145], s[46:47], 0, v[142:143]
	s_add_i32 m0, s20, 0xe000
	s_nop 0
	global_load_lds_dwordx4 v[144:145], off

.Lrxp_relu2_w0:
	s_waitcnt vmcnt(24)
	s_waitcnt lgkmcnt(0)
	s_barrier
	s_setprio 1
	s_waitcnt lgkmcnt(0)
	v_mfma_f32_16x16x32_bf16 v[128:131], v[148:151], v[198:201], 0
	v_mfma_f32_16x16x32_bf16 v[124:127], v[158:161], v[198:201], 0
	v_mfma_f32_16x16x32_bf16 v[110:113], v[148:151], v[206:209], 0
	v_mfma_f32_16x16x32_bf16 v[106:109], v[158:161], v[206:209], 0
	v_mfma_f32_16x16x32_bf16 v[94:97], v[148:151], v[214:217], 0
	v_mfma_f32_16x16x32_bf16 v[90:93], v[158:161], v[214:217], 0
	v_mfma_f32_16x16x32_bf16 v[78:81], v[148:151], v[222:225], 0
	v_mfma_f32_16x16x32_bf16 v[74:77], v[158:161], v[222:225], 0
	v_mfma_f32_16x16x32_bf16 v[128:131], v[152:155], v[202:205], v[128:131]
	v_mfma_f32_16x16x32_bf16 v[124:127], v[166:169], v[202:205], v[124:127]
	v_mfma_f32_16x16x32_bf16 v[110:113], v[152:155], v[210:213], v[110:113]
	v_mfma_f32_16x16x32_bf16 v[106:109], v[166:169], v[210:213], v[106:109]
	v_mfma_f32_16x16x32_bf16 v[94:97], v[152:155], v[218:221], v[94:97]
	v_mfma_f32_16x16x32_bf16 v[90:93], v[166:169], v[218:221], v[90:93]
	v_mfma_f32_16x16x32_bf16 v[78:81], v[152:155], v[226:229], v[78:81]
	v_mfma_f32_16x16x32_bf16 v[74:77], v[166:169], v[226:229], v[74:77]
	s_setprio 0
	s_setprio 1
	v_mfma_f32_16x16x32_bf16 v[120:123], v[170:173], v[198:201], 0
	v_mfma_f32_16x16x32_bf16 v[116:119], v[178:181], v[198:201], 0
	v_mfma_f32_16x16x32_bf16 v[102:105], v[170:173], v[206:209], 0
	v_mfma_f32_16x16x32_bf16 v[98:101], v[178:181], v[206:209], 0
	v_mfma_f32_16x16x32_bf16 v[86:89], v[170:173], v[214:217], 0
	v_mfma_f32_16x16x32_bf16 v[82:85], v[178:181], v[214:217], 0
	v_mfma_f32_16x16x32_bf16 v[70:73], v[170:173], v[222:225], 0
	v_mfma_f32_16x16x32_bf16 v[66:69], v[178:181], v[222:225], 0
	v_mfma_f32_16x16x32_bf16 v[120:123], v[174:177], v[202:205], v[120:123]
	v_mfma_f32_16x16x32_bf16 v[116:119], v[194:197], v[202:205], v[116:119]
	v_mfma_f32_16x16x32_bf16 v[102:105], v[174:177], v[210:213], v[102:105]
	v_mfma_f32_16x16x32_bf16 v[98:101], v[194:197], v[210:213], v[98:101]
	v_mfma_f32_16x16x32_bf16 v[86:89], v[174:177], v[218:221], v[86:89]
	v_mfma_f32_16x16x32_bf16 v[82:85], v[194:197], v[218:221], v[82:85]
	v_mfma_f32_16x16x32_bf16 v[70:73], v[174:177], v[226:229], v[70:73]
	v_mfma_f32_16x16x32_bf16 v[66:69], v[194:197], v[226:229], v[66:69]
	s_setprio 0
	s_barrier
	s_add_i32 s16, s16, s7
	v_lshl_add_u64 v[144:145], s[50:51], 0, v[114:115]
	s_mov_b32 m0, s16
	ds_read_b128 v[198:201], v147 offset:16384
	ds_read_b128 v[202:205], v147 offset:17408
	ds_read_b128 v[206:209], v147 offset:18432
	ds_read_b128 v[210:213], v147 offset:19456
	ds_read_b128 v[214:217], v147 offset:20480
	ds_read_b128 v[218:221], v147 offset:21504
	ds_read_b128 v[222:225], v147 offset:22528
	ds_read_b128 v[226:229], v147 offset:23552
	global_load_lds_dwordx4 v[144:145], off
	s_add_i32 m0, s16, 0x2000
	s_add_u32 s16, s50, 0x1000
	v_lshl_add_u64 v[144:145], s[50:51], 0, v[136:137]
	s_addc_u32 s17, s51, 0
	s_add_i32 s65, s65, s7
	global_load_lds_dwordx4 v[144:145], off
	v_lshl_add_u64 v[144:145], s[16:17], 0, v[114:115]
	s_mov_b32 m0, s65
	s_nop 0
	global_load_lds_dwordx4 v[144:145], off
	v_lshl_add_u64 v[144:145], s[16:17], 0, v[136:137]
	s_add_i32 m0, s65, 0x2000
	s_nop 0
	global_load_lds_dwordx4 v[144:145], off
	v_lshl_add_u64 v[144:145], s[52:53], 0, v[132:133]
	s_mov_b32 m0, s20
	s_nop 0
	global_load_lds_dwordx4 v[144:145], off
	v_lshl_add_u64 v[144:145], s[52:53], 0, v[134:135]
	s_mov_b32 m0, s21
	s_nop 0
	global_load_lds_dwordx4 v[144:145], off
	s_cmp_lg_u32 s32, 0
	s_cbranch_scc1 .Lrxp_relu2_w1
	s_waitcnt vmcnt(8)
.Lrxp_relu2_w1:
	s_waitcnt vmcnt(24)
	s_waitcnt lgkmcnt(0)
	s_barrier
	s_setprio 1
	s_waitcnt lgkmcnt(0)
	v_mfma_f32_16x16x32_bf16 v[62:65], v[148:151], v[198:201], 0
	v_mfma_f32_16x16x32_bf16 v[58:61], v[158:161], v[198:201], 0
	v_mfma_f32_16x16x32_bf16 v[46:49], v[148:151], v[206:209], 0
	v_mfma_f32_16x16x32_bf16 v[42:45], v[158:161], v[206:209], 0
	v_mfma_f32_16x16x32_bf16 v[30:33], v[148:151], v[214:217], 0
	v_mfma_f32_16x16x32_bf16 v[26:29], v[158:161], v[214:217], 0
	v_mfma_f32_16x16x32_bf16 v[14:17], v[148:151], v[222:225], 0
	v_mfma_f32_16x16x32_bf16 v[10:13], v[158:161], v[222:225], 0
	v_mfma_f32_16x16x32_bf16 v[62:65], v[152:155], v[202:205], v[62:65]
	v_mfma_f32_16x16x32_bf16 v[58:61], v[166:169], v[202:205], v[58:61]
	v_mfma_f32_16x16x32_bf16 v[46:49], v[152:155], v[210:213], v[46:49]
	v_mfma_f32_16x16x32_bf16 v[42:45], v[166:169], v[210:213], v[42:45]
	v_mfma_f32_16x16x32_bf16 v[30:33], v[152:155], v[218:221], v[30:33]
	v_mfma_f32_16x16x32_bf16 v[26:29], v[166:169], v[218:221], v[26:29]
	v_mfma_f32_16x16x32_bf16 v[14:17], v[152:155], v[226:229], v[14:17]
	v_mfma_f32_16x16x32_bf16 v[10:13], v[166:169], v[226:229], v[10:13]
	s_setprio 0
	s_setprio 1
	v_mfma_f32_16x16x32_bf16 v[54:57], v[170:173], v[198:201], 0
	v_mfma_f32_16x16x32_bf16 v[50:53], v[178:181], v[198:201], 0
	v_mfma_f32_16x16x32_bf16 v[38:41], v[170:173], v[206:209], 0
	v_mfma_f32_16x16x32_bf16 v[34:37], v[178:181], v[206:209], 0
	v_mfma_f32_16x16x32_bf16 v[22:25], v[170:173], v[214:217], 0
	v_mfma_f32_16x16x32_bf16 v[18:21], v[178:181], v[214:217], 0
	v_mfma_f32_16x16x32_bf16 v[6:9], v[170:173], v[222:225], 0
	v_mfma_f32_16x16x32_bf16 v[2:5], v[178:181], v[222:225], 0
	v_mfma_f32_16x16x32_bf16 v[54:57], v[174:177], v[202:205], v[54:57]
	v_mfma_f32_16x16x32_bf16 v[50:53], v[194:197], v[202:205], v[50:53]
	v_mfma_f32_16x16x32_bf16 v[38:41], v[174:177], v[210:213], v[38:41]
	v_mfma_f32_16x16x32_bf16 v[34:37], v[194:197], v[210:213], v[34:37]
	v_mfma_f32_16x16x32_bf16 v[22:25], v[174:177], v[218:221], v[22:25]
	v_mfma_f32_16x16x32_bf16 v[18:21], v[194:197], v[218:221], v[18:21]
	v_mfma_f32_16x16x32_bf16 v[6:9], v[174:177], v[226:229], v[6:9]
	v_mfma_f32_16x16x32_bf16 v[2:5], v[194:197], v[226:229], v[2:5]
	s_setprio 0
	s_barrier
	s_add_i32 s65, 0, 0x18000
	v_add_u32_e32 v144, s65, v1
	s_add_i32 s66, 0, 0x1c000
	ds_read_b128 v[148:151], v144
	ds_read_b128 v[152:155], v144 offset:1024
	ds_read_b128 v[158:161], v144 offset:2048
	ds_read_b128 v[166:169], v144 offset:3072
	v_add_u32_e32 v144, s66, v1
	ds_read_b128 v[170:173], v144
	ds_read_b128 v[174:177], v144 offset:1024
	ds_read_b128 v[178:181], v144 offset:2048
	ds_read_b128 v[194:197], v144 offset:3072
	s_add_u32 s16, s52, 0x4000
	s_addc_u32 s17, s53, 0
	s_mov_b32 m0, s24
	v_lshl_add_u64 v[144:145], s[16:17], 0, v[132:133]
	ds_read_b128 v[198:201], v147 offset:32768
	ds_read_b128 v[202:205], v147 offset:33792
	ds_read_b128 v[206:209], v147 offset:34816
	ds_read_b128 v[210:213], v147 offset:35840
	ds_read_b128 v[214:217], v147 offset:36864
	ds_read_b128 v[218:221], v147 offset:37888
	ds_read_b128 v[222:225], v147 offset:38912
	ds_read_b128 v[226:229], v147 offset:39936
	global_load_lds_dwordx4 v[144:145], off
	v_lshl_add_u64 v[144:145], s[16:17], 0, v[134:135]
	s_mov_b32 m0, s37
	s_nop 0
	global_load_lds_dwordx4 v[144:145], off
	s_cmp_lg_u32 s32, 0
	s_cbranch_scc1 .Lrxp_relu2_w2
	s_waitcnt vmcnt(8)
.Lrxp_relu2_w2:
	s_waitcnt vmcnt(24)
	s_mov_b32 s32, 0
	s_waitcnt lgkmcnt(0)
	s_barrier
	s_setprio 1
	s_waitcnt lgkmcnt(0)
	v_mfma_f32_16x16x32_bf16 v[128:131], v[148:151], v[198:201], v[128:131]
	v_mfma_f32_16x16x32_bf16 v[124:127], v[158:161], v[198:201], v[124:127]
	v_mfma_f32_16x16x32_bf16 v[110:113], v[148:151], v[206:209], v[110:113]
	v_mfma_f32_16x16x32_bf16 v[106:109], v[158:161], v[206:209], v[106:109]
	v_mfma_f32_16x16x32_bf16 v[94:97], v[148:151], v[214:217], v[94:97]
	v_mfma_f32_16x16x32_bf16 v[90:93], v[158:161], v[214:217], v[90:93]
	v_mfma_f32_16x16x32_bf16 v[78:81], v[148:151], v[222:225], v[78:81]
	v_mfma_f32_16x16x32_bf16 v[74:77], v[158:161], v[222:225], v[74:77]
	v_mfma_f32_16x16x32_bf16 v[128:131], v[152:155], v[202:205], v[128:131]
	v_mfma_f32_16x16x32_bf16 v[124:127], v[166:169], v[202:205], v[124:127]
	v_mfma_f32_16x16x32_bf16 v[110:113], v[152:155], v[210:213], v[110:113]
	v_mfma_f32_16x16x32_bf16 v[106:109], v[166:169], v[210:213], v[106:109]
	v_mfma_f32_16x16x32_bf16 v[94:97], v[152:155], v[218:221], v[94:97]
	v_mfma_f32_16x16x32_bf16 v[90:93], v[166:169], v[218:221], v[90:93]
	v_mfma_f32_16x16x32_bf16 v[78:81], v[152:155], v[226:229], v[78:81]
	v_mfma_f32_16x16x32_bf16 v[74:77], v[166:169], v[226:229], v[74:77]
	s_setprio 0
	s_setprio 1
	v_mfma_f32_16x16x32_bf16 v[120:123], v[170:173], v[198:201], v[120:123]
	v_mfma_f32_16x16x32_bf16 v[116:119], v[178:181], v[198:201], v[116:119]
	v_mfma_f32_16x16x32_bf16 v[102:105], v[170:173], v[206:209], v[102:105]
	v_mfma_f32_16x16x32_bf16 v[98:101], v[178:181], v[206:209], v[98:101]
	v_mfma_f32_16x16x32_bf16 v[86:89], v[170:173], v[214:217], v[86:89]
	v_mfma_f32_16x16x32_bf16 v[82:85], v[178:181], v[214:217], v[82:85]
	v_mfma_f32_16x16x32_bf16 v[70:73], v[170:173], v[222:225], v[70:73]
	v_mfma_f32_16x16x32_bf16 v[66:69], v[178:181], v[222:225], v[66:69]
	v_mfma_f32_16x16x32_bf16 v[120:123], v[174:177], v[202:205], v[120:123]
	v_mfma_f32_16x16x32_bf16 v[116:119], v[194:197], v[202:205], v[116:119]
	v_mfma_f32_16x16x32_bf16 v[102:105], v[174:177], v[210:213], v[102:105]
	v_mfma_f32_16x16x32_bf16 v[98:101], v[194:197], v[210:213], v[98:101]
	v_mfma_f32_16x16x32_bf16 v[86:89], v[174:177], v[218:221], v[86:89]
	v_mfma_f32_16x16x32_bf16 v[82:85], v[194:197], v[218:221], v[82:85]
	v_mfma_f32_16x16x32_bf16 v[70:73], v[174:177], v[226:229], v[70:73]
	v_mfma_f32_16x16x32_bf16 v[66:69], v[194:197], v[226:229], v[66:69]
	s_setprio 0
	s_barrier
	s_add_u32 s16, s50, 0x8000
	s_addc_u32 s17, s51, 0
	s_add_i32 s52, s65, s7
	v_lshl_add_u64 v[144:145], s[16:17], 0, v[114:115]
	s_mov_b32 m0, s52
	ds_read_b128 v[198:201], v147 offset:49152
	ds_read_b128 v[202:205], v147 offset:50176
	ds_read_b128 v[206:209], v147 offset:51200
	ds_read_b128 v[210:213], v147 offset:52224
	ds_read_b128 v[214:217], v147 offset:53248
	ds_read_b128 v[218:221], v147 offset:54272
	ds_read_b128 v[222:225], v147 offset:55296
	ds_read_b128 v[226:229], v147 offset:56320
	global_load_lds_dwordx4 v[144:145], off
	s_add_i32 m0, s52, 0x2000
	v_lshl_add_u64 v[144:145], s[16:17], 0, v[136:137]
	s_add_u32 s16, s50, 0x9000
	s_addc_u32 s17, s51, 0
	s_add_i32 s50, s66, s7
	global_load_lds_dwordx4 v[144:145], off
	v_lshl_add_u64 v[144:145], s[16:17], 0, v[114:115]
	s_mov_b32 m0, s50
	s_nop 0
	global_load_lds_dwordx4 v[144:145], off
	v_lshl_add_u64 v[144:145], s[16:17], 0, v[136:137]
	s_add_i32 m0, s50, 0x2000
	s_nop 0
	global_load_lds_dwordx4 v[144:145], off
	v_lshl_add_u64 v[144:145], s[48:49], 0, v[132:133]
	s_mov_b32 m0, s54
	s_nop 0
	global_load_lds_dwordx4 v[144:145], off
	v_lshl_add_u64 v[144:145], s[48:49], 0, v[134:135]
	s_mov_b32 m0, s55
	s_nop 0
	global_load_lds_dwordx4 v[144:145], off
	s_waitcnt vmcnt(8)
	s_waitcnt lgkmcnt(0)
	s_barrier
	s_setprio 1
	s_waitcnt lgkmcnt(0)
	v_mfma_f32_16x16x32_bf16 v[62:65], v[148:151], v[198:201], v[62:65]
	v_mfma_f32_16x16x32_bf16 v[58:61], v[158:161], v[198:201], v[58:61]
	v_mfma_f32_16x16x32_bf16 v[46:49], v[148:151], v[206:209], v[46:49]
	v_mfma_f32_16x16x32_bf16 v[42:45], v[158:161], v[206:209], v[42:45]
	v_mfma_f32_16x16x32_bf16 v[30:33], v[148:151], v[214:217], v[30:33]
	v_mfma_f32_16x16x32_bf16 v[26:29], v[158:161], v[214:217], v[26:29]
	v_mfma_f32_16x16x32_bf16 v[14:17], v[148:151], v[222:225], v[14:17]
	v_mfma_f32_16x16x32_bf16 v[10:13], v[158:161], v[222:225], v[10:13]
	v_mfma_f32_16x16x32_bf16 v[62:65], v[152:155], v[202:205], v[62:65]
	v_mfma_f32_16x16x32_bf16 v[58:61], v[166:169], v[202:205], v[58:61]
	v_mfma_f32_16x16x32_bf16 v[46:49], v[152:155], v[210:213], v[46:49]
	v_mfma_f32_16x16x32_bf16 v[42:45], v[166:169], v[210:213], v[42:45]
	v_mfma_f32_16x16x32_bf16 v[30:33], v[152:155], v[218:221], v[30:33]
	v_mfma_f32_16x16x32_bf16 v[26:29], v[166:169], v[218:221], v[26:29]
	v_mfma_f32_16x16x32_bf16 v[14:17], v[152:155], v[226:229], v[14:17]
	v_mfma_f32_16x16x32_bf16 v[10:13], v[166:169], v[226:229], v[10:13]
	s_setprio 0
	s_setprio 1
	v_mfma_f32_16x16x32_bf16 v[54:57], v[170:173], v[198:201], v[54:57]
	v_mfma_f32_16x16x32_bf16 v[50:53], v[178:181], v[198:201], v[50:53]
	v_mfma_f32_16x16x32_bf16 v[38:41], v[170:173], v[206:209], v[38:41]
	v_mfma_f32_16x16x32_bf16 v[34:37], v[178:181], v[206:209], v[34:37]
	v_mfma_f32_16x16x32_bf16 v[22:25], v[170:173], v[214:217], v[22:25]
	v_mfma_f32_16x16x32_bf16 v[18:21], v[178:181], v[214:217], v[18:21]
	v_mfma_f32_16x16x32_bf16 v[6:9], v[170:173], v[222:225], v[6:9]
	v_mfma_f32_16x16x32_bf16 v[2:5], v[178:181], v[222:225], v[2:5]
	v_mfma_f32_16x16x32_bf16 v[54:57], v[174:177], v[202:205], v[54:57]
	v_mfma_f32_16x16x32_bf16 v[50:53], v[194:197], v[202:205], v[50:53]
	v_mfma_f32_16x16x32_bf16 v[38:41], v[174:177], v[210:213], v[38:41]
	v_mfma_f32_16x16x32_bf16 v[34:37], v[194:197], v[210:213], v[34:37]
	v_mfma_f32_16x16x32_bf16 v[22:25], v[174:177], v[218:221], v[22:25]
	v_mfma_f32_16x16x32_bf16 v[18:21], v[194:197], v[218:221], v[18:21]
	v_mfma_f32_16x16x32_bf16 v[6:9], v[174:177], v[226:229], v[6:9]
	v_mfma_f32_16x16x32_bf16 v[2:5], v[194:197], v[226:229], v[2:5]
	s_setprio 0
	s_barrier
	s_add_i32 s64, s64, 2
	s_add_u32 s46, s46, 0x10000
	s_addc_u32 s47, s47, 0
	s_add_u32 s62, s62, 0x10000
	s_addc_u32 s63, s63, 0
	s_cmp_gt_u32 s64, 29
	s_cbranch_scc0 .LBB0_1230
	s_branch .Lpeel_exit_relu2

.Lpeel_exit_relu2:
	s_add_u32 s100, s60, 0xc000
	s_addc_u32 s101, s29, 0
	v_lshl_add_u64 v[144:145], s[100:101], 0, v[140:141]
	s_add_i32 m0, s20, 0xc000
	s_nop 0
	global_load_lds_dwordx4 v[144:145], off
	v_lshl_add_u64 v[144:145], s[100:101], 0, v[142:143]
	s_add_i32 m0, s20, 0xe000
	s_nop 0
	global_load_lds_dwordx4 v[144:145], off
	s_and_b64 vcc, exec, s[10:11]
	s_cbranch_vccz .LBB0_1233
	s_barrier
